# speedup vs baseline: 1.0062x; 1.0062x over previous
.LBB0_21:
	v_exp_f32_e64 v156, -|v154|
	v_max_f32 v157, 0, v154
	v_add_f32 v156, 1.0, v156
	v_log_f32 v156, v156
	s_nop 0
	v_fma_mixlo_f16 v155, v156, 1.0, v157
	ds_write_b16 v148, v155
	v_mov_b32_e32 v192, v106
	v_mov_b32_e32 v193, v110
	v_mul_f32 v182, -2.0, v153
	s_nop 6
	ds_read_b128 v[208:211], v139
	s_waitcnt lgkmcnt(1)
	s_barrier
	ds_read_b128 v[212:215], v140
	ds_read_b128 v[216:219], v141
	s_waitcnt lgkmcnt(2)
	v_smfmac_f32_16x16x64_f16 v[192:195], v[208:211], v[6:13], v191
	ds_read_b128 v[220:223], v142
	s_waitcnt lgkmcnt(2)
	v_smfmac_f32_16x16x64_f16 v[192:195], v[212:215], v[14:21], v191
	s_waitcnt lgkmcnt(1)
	v_smfmac_f32_16x16x64_f16 v[192:195], v[216:219], v[26:33], v191
	s_waitcnt lgkmcnt(0)
	v_smfmac_f32_16x16x64_f16 v[192:195], v[220:223], v[34:41], v191
	s_nop 7
	v_cndmask_b32_e64 v154, v192, v193, s[0:1]
	v_exp_f32_e64 v156, -|v154|
	v_max_f32 v157, 0, v154
	v_add_f32 v156, 1.0, v156
	v_log_f32 v156, v156
	s_nop 0
	v_fma_mixlo_f16 v155, v156, 1.0, v157
	ds_write_b16 v149, v155
	v_mov_b32_e32 v200, v114
	v_mov_b32_e32 v201, v118
	v_mov_b32_e32 v204, v122
	v_mov_b32_e32 v205, v126
	s_nop 2
	ds_read_b128 v[208:211], v143
	s_waitcnt lgkmcnt(1)
	s_barrier
	ds_read_b128 v[212:215], v144
	ds_read_b128 v[216:219], v145
	s_waitcnt lgkmcnt(2)
	v_smfmac_f32_16x16x64_f16 v[200:203], v[208:211], v[42:49], v191
	ds_read_b128 v[220:223], v146
	v_smfmac_f32_16x16x64_f16 v[204:207], v[208:211], v[74:81], v191
	s_waitcnt lgkmcnt(2)
	v_smfmac_f32_16x16x64_f16 v[200:203], v[212:215], v[50:57], v191
	v_smfmac_f32_16x16x64_f16 v[204:207], v[212:215], v[82:89], v191
	s_waitcnt lgkmcnt(1)
	v_smfmac_f32_16x16x64_f16 v[200:203], v[216:219], v[58:65], v191
	v_smfmac_f32_16x16x64_f16 v[204:207], v[216:219], v[90:97], v191
	s_waitcnt lgkmcnt(0)
	v_smfmac_f32_16x16x64_f16 v[200:203], v[220:223], v[66:73], v191
	v_smfmac_f32_16x16x64_f16 v[204:207], v[220:223], v[98:105], v191
	s_nop 6
	v_cndmask_b32_e64 v170, v201, v200, s[6:7]
	v_cndmask_b32_e64 v170, v170, v204, s[0:1]
	v_cndmask_b32_e64 v170, v170, v205, s[4:5]
	v_exp_f32_e32 v170, v170
	s_nop 0
	v_add_f32_e32 v170, 1.0, v170
	v_rcp_f32_e32 v170, v170
	s_nop 0
	v_fmac_f32_e32 v153, v170, v182
	s_nop 1
	v_add_f32_dpp v153, v153, v153 quad_perm:[1,0,3,2] row_mask:0xf bank_mask:0xf bound_ctrl:1
	s_nop 1
	v_add_f32_dpp v153, v153, v153 quad_perm:[2,3,0,1] row_mask:0xf bank_mask:0xf bound_ctrl:1
	s_nop 1
	v_add_f32_dpp v153, v153, v153 row_half_mirror row_mask:0xf bank_mask:0xf bound_ctrl:1
	v_cvt_f16_f32_e32 v170, v153
	ds_write_b16 v150, v170
	s_waitcnt lgkmcnt(0)
	s_barrier
	ds_read_b128 v[154:157], v147
	s_waitcnt lgkmcnt(0)
	v_smfmac_f32_16x16x64_f16 v[130:133], v[154:157], v[248:255], v191
	s_nop 2
	v_add_u32_e32 v134, s3, v151
	ds_read_b32 v135, v134
	s_nop 2
	v_cndmask_b32_e64 v136, v130, v131, s[0:1]
	v_exp_f32_e64 v158, -|v136|
	v_max_f32 v159, 0, v136
	v_add_f32 v158, 1.0, v158
	v_log_f32 v158, v158
	s_nop 0
	v_fma_mixlo_f16 v137, v158, 1.0, v159
	ds_write_b16 v148, v137
	v_mov_b32_e32 v192, v106
	v_mov_b32_e32 v193, v110
	v_add_f32_e32 v136, v152, v153
	v_mul_f32 v137, -2.0, v135
	s_nop 6
	ds_read_b128 v[208:211], v139
	s_waitcnt lgkmcnt(1)
	s_barrier
	ds_read_b128 v[212:215], v140
	ds_read_b128 v[216:219], v141
	s_waitcnt lgkmcnt(2)
	v_smfmac_f32_16x16x64_f16 v[192:195], v[208:211], v[6:13], v191
	ds_read_b128 v[220:223], v142
	s_waitcnt lgkmcnt(2)
	v_smfmac_f32_16x16x64_f16 v[192:195], v[212:215], v[14:21], v191
	s_waitcnt lgkmcnt(1)
	v_smfmac_f32_16x16x64_f16 v[192:195], v[216:219], v[26:33], v191
	s_waitcnt lgkmcnt(0)
	v_smfmac_f32_16x16x64_f16 v[192:195], v[220:223], v[34:41], v191
	s_nop 7
	v_cndmask_b32_e64 v152, v192, v193, s[0:1]
	v_exp_f32_e64 v158, -|v152|
	v_max_f32 v159, 0, v152
	v_add_f32 v158, 1.0, v158
	v_log_f32 v158, v158
	s_nop 0
	v_fma_mixlo_f16 v153, v158, 1.0, v159
	ds_write_b16 v149, v153
	v_mov_b32_e32 v200, v114
	v_mov_b32_e32 v201, v118
	v_mov_b32_e32 v204, v122
	v_mov_b32_e32 v205, v126
	s_nop 2
	ds_read_b128 v[208:211], v143
	s_waitcnt lgkmcnt(1)
	s_barrier
	ds_read_b128 v[212:215], v144
	ds_read_b128 v[216:219], v145
	s_waitcnt lgkmcnt(2)
	v_smfmac_f32_16x16x64_f16 v[200:203], v[208:211], v[42:49], v191
	ds_read_b128 v[220:223], v146
	v_smfmac_f32_16x16x64_f16 v[204:207], v[208:211], v[74:81], v191
	s_waitcnt lgkmcnt(2)
	v_smfmac_f32_16x16x64_f16 v[200:203], v[212:215], v[50:57], v191
	v_smfmac_f32_16x16x64_f16 v[204:207], v[212:215], v[82:89], v191
	s_waitcnt lgkmcnt(1)
	v_smfmac_f32_16x16x64_f16 v[200:203], v[216:219], v[58:65], v191
	v_smfmac_f32_16x16x64_f16 v[204:207], v[216:219], v[90:97], v191
	s_waitcnt lgkmcnt(0)
	v_smfmac_f32_16x16x64_f16 v[200:203], v[220:223], v[66:73], v191
	v_smfmac_f32_16x16x64_f16 v[204:207], v[220:223], v[98:105], v191
	s_nop 6
	v_cndmask_b32_e64 v152, v201, v200, s[6:7]
	v_cndmask_b32_e64 v152, v152, v204, s[0:1]
	v_cndmask_b32_e64 v152, v152, v205, s[4:5]
	v_exp_f32_e32 v152, v152
	s_nop 0
	v_add_f32_e32 v152, 1.0, v152
	v_rcp_f32_e32 v152, v152
	s_nop 0
	v_fmac_f32_e32 v135, v152, v137
	s_nop 1
	v_add_f32_dpp v135, v135, v135 quad_perm:[1,0,3,2] row_mask:0xf bank_mask:0xf bound_ctrl:1
	s_nop 1
	v_add_f32_dpp v135, v135, v135 quad_perm:[2,3,0,1] row_mask:0xf bank_mask:0xf bound_ctrl:1
	s_nop 1
	v_add_f32_dpp v135, v135, v135 row_half_mirror row_mask:0xf bank_mask:0xf bound_ctrl:1
	v_cvt_f16_f32_e32 v137, v135
	ds_write_b16 v150, v137
	s_waitcnt lgkmcnt(0)
	s_barrier
	ds_read_b128 v[158:161], v147
	ds_read_b32 v137, v134 offset:32
	v_add_f32_e32 v135, v136, v135
	s_waitcnt lgkmcnt(1)
	v_smfmac_f32_16x16x64_f16 v[130:133], v[158:161], v[248:255], v191
	s_nop 7
	v_cndmask_b32_e64 v156, v130, v131, s[0:1]
	v_exp_f32_e64 v158, -|v156|
	v_max_f32 v159, 0, v156
	v_add_f32 v158, 1.0, v158
	v_log_f32 v158, v158
	s_nop 0
	v_fma_mixlo_f16 v157, v158, 1.0, v159
	ds_write_b16 v148, v157
	v_mov_b32_e32 v192, v106
	v_mov_b32_e32 v193, v110
	v_mul_f32 v136, -2.0, v137
	s_nop 6
	ds_read_b128 v[208:211], v139
	s_waitcnt lgkmcnt(1)
	s_barrier
	ds_read_b128 v[212:215], v140
	ds_read_b128 v[216:219], v141
	s_waitcnt lgkmcnt(2)
	v_smfmac_f32_16x16x64_f16 v[192:195], v[208:211], v[6:13], v191
	ds_read_b128 v[220:223], v142
	s_waitcnt lgkmcnt(2)
	v_smfmac_f32_16x16x64_f16 v[192:195], v[212:215], v[14:21], v191
	s_waitcnt lgkmcnt(1)
	v_smfmac_f32_16x16x64_f16 v[192:195], v[216:219], v[26:33], v191
	s_waitcnt lgkmcnt(0)
	v_smfmac_f32_16x16x64_f16 v[192:195], v[220:223], v[34:41], v191
	s_nop 7
	v_cndmask_b32_e64 v156, v192, v193, s[0:1]
	v_exp_f32_e64 v158, -|v156|
	v_max_f32 v159, 0, v156
	v_add_f32 v158, 1.0, v158
	v_log_f32 v158, v158
	s_nop 0
	v_fma_mixlo_f16 v157, v158, 1.0, v159
	ds_write_b16 v149, v157
	v_mov_b32_e32 v200, v114
	v_mov_b32_e32 v201, v118
	v_mov_b32_e32 v204, v122
	v_mov_b32_e32 v205, v126
	s_nop 2
	ds_read_b128 v[208:211], v143
	s_waitcnt lgkmcnt(1)
	s_barrier
	ds_read_b128 v[212:215], v144
	ds_read_b128 v[216:219], v145
	s_waitcnt lgkmcnt(2)
	v_smfmac_f32_16x16x64_f16 v[200:203], v[208:211], v[42:49], v191
	ds_read_b128 v[220:223], v146
	v_smfmac_f32_16x16x64_f16 v[204:207], v[208:211], v[74:81], v191
	s_waitcnt lgkmcnt(2)
	v_smfmac_f32_16x16x64_f16 v[200:203], v[212:215], v[50:57], v191
	v_smfmac_f32_16x16x64_f16 v[204:207], v[212:215], v[82:89], v191
	s_waitcnt lgkmcnt(1)
	v_smfmac_f32_16x16x64_f16 v[200:203], v[216:219], v[58:65], v191
	v_smfmac_f32_16x16x64_f16 v[204:207], v[216:219], v[90:97], v191
	s_waitcnt lgkmcnt(0)
	v_smfmac_f32_16x16x64_f16 v[200:203], v[220:223], v[66:73], v191
	v_smfmac_f32_16x16x64_f16 v[204:207], v[220:223], v[98:105], v191
	s_nop 6
	v_cndmask_b32_e64 v172, v201, v200, s[6:7]
	v_cndmask_b32_e64 v172, v172, v204, s[0:1]
	v_cndmask_b32_e64 v172, v172, v205, s[4:5]
	v_exp_f32_e32 v172, v172
	s_nop 0
	v_add_f32_e32 v172, 1.0, v172
	v_rcp_f32_e32 v172, v172
	s_nop 0
	v_fmac_f32_e32 v137, v172, v136
	s_nop 1
	v_add_f32_dpp v136, v137, v137 quad_perm:[1,0,3,2] row_mask:0xf bank_mask:0xf bound_ctrl:1
	s_nop 1
	v_add_f32_dpp v136, v136, v136 quad_perm:[2,3,0,1] row_mask:0xf bank_mask:0xf bound_ctrl:1
	s_nop 1
	v_add_f32_dpp v136, v136, v136 row_half_mirror row_mask:0xf bank_mask:0xf bound_ctrl:1
	v_cvt_f16_f32_e32 v137, v136
	ds_write_b16 v150, v137
	s_waitcnt lgkmcnt(0)
	s_barrier
	ds_read_b128 v[156:159], v147
	ds_read_b32 v137, v134 offset:64
	v_add_f32_e32 v135, v135, v136
	s_waitcnt lgkmcnt(1)
	v_smfmac_f32_16x16x64_f16 v[130:133], v[156:159], v[248:255], v191
	s_nop 7
	v_cndmask_b32_e64 v156, v130, v131, s[0:1]
	v_exp_f32_e64 v158, -|v156|
	v_max_f32 v159, 0, v156
	v_add_f32 v158, 1.0, v158
	v_log_f32 v158, v158
	s_nop 0
	v_fma_mixlo_f16 v157, v158, 1.0, v159
	ds_write_b16 v148, v157
	v_mov_b32_e32 v192, v106
	v_mov_b32_e32 v193, v110
	v_mul_f32 v136, -2.0, v137
	s_nop 6
	ds_read_b128 v[208:211], v139
	s_waitcnt lgkmcnt(1)
	s_barrier
	ds_read_b128 v[212:215], v140
	ds_read_b128 v[216:219], v141
	s_waitcnt lgkmcnt(2)
	v_smfmac_f32_16x16x64_f16 v[192:195], v[208:211], v[6:13], v191
	ds_read_b128 v[220:223], v142
	s_waitcnt lgkmcnt(2)
	v_smfmac_f32_16x16x64_f16 v[192:195], v[212:215], v[14:21], v191
	s_waitcnt lgkmcnt(1)
	v_smfmac_f32_16x16x64_f16 v[192:195], v[216:219], v[26:33], v191
	s_waitcnt lgkmcnt(0)
	v_smfmac_f32_16x16x64_f16 v[192:195], v[220:223], v[34:41], v191
	s_nop 7
	v_cndmask_b32_e64 v156, v192, v193, s[0:1]
	v_exp_f32_e64 v158, -|v156|
	v_max_f32 v159, 0, v156
	v_add_f32 v158, 1.0, v158
	v_log_f32 v158, v158
	s_nop 0
	v_fma_mixlo_f16 v157, v158, 1.0, v159
	ds_write_b16 v149, v157
	v_mov_b32_e32 v200, v114
	v_mov_b32_e32 v201, v118
	v_mov_b32_e32 v204, v122
	v_mov_b32_e32 v205, v126
	s_nop 2
	ds_read_b128 v[208:211], v143
	s_waitcnt lgkmcnt(1)
	s_barrier
	ds_read_b128 v[212:215], v144
	ds_read_b128 v[216:219], v145
	s_waitcnt lgkmcnt(2)
	v_smfmac_f32_16x16x64_f16 v[200:203], v[208:211], v[42:49], v191
	ds_read_b128 v[220:223], v146
	v_smfmac_f32_16x16x64_f16 v[204:207], v[208:211], v[74:81], v191
	s_waitcnt lgkmcnt(2)
	v_smfmac_f32_16x16x64_f16 v[200:203], v[212:215], v[50:57], v191
	v_smfmac_f32_16x16x64_f16 v[204:207], v[212:215], v[82:89], v191
	s_waitcnt lgkmcnt(1)
	v_smfmac_f32_16x16x64_f16 v[200:203], v[216:219], v[58:65], v191
	v_smfmac_f32_16x16x64_f16 v[204:207], v[216:219], v[90:97], v191
	s_waitcnt lgkmcnt(0)
	v_smfmac_f32_16x16x64_f16 v[200:203], v[220:223], v[66:73], v191
	v_smfmac_f32_16x16x64_f16 v[204:207], v[220:223], v[98:105], v191
	s_nop 6
	v_cndmask_b32_e64 v172, v201, v200, s[6:7]
	v_cndmask_b32_e64 v172, v172, v204, s[0:1]
	v_cndmask_b32_e64 v172, v172, v205, s[4:5]
	v_exp_f32_e32 v172, v172
	s_nop 0
	v_add_f32_e32 v172, 1.0, v172
	v_rcp_f32_e32 v172, v172
	s_nop 0
	v_fmac_f32_e32 v137, v172, v136
	s_nop 1
	v_add_f32_dpp v136, v137, v137 quad_perm:[1,0,3,2] row_mask:0xf bank_mask:0xf bound_ctrl:1
	s_nop 1
	v_add_f32_dpp v136, v136, v136 quad_perm:[2,3,0,1] row_mask:0xf bank_mask:0xf bound_ctrl:1
	s_nop 1
	v_add_f32_dpp v136, v136, v136 row_half_mirror row_mask:0xf bank_mask:0xf bound_ctrl:1
	v_cvt_f16_f32_e32 v137, v136
	ds_write_b16 v150, v137
	s_waitcnt lgkmcnt(0)
	s_barrier
	ds_read_b128 v[156:159], v147
	ds_read_b32 v137, v134 offset:96
	v_add_f32_e32 v135, v135, v136
	s_waitcnt lgkmcnt(1)
	v_smfmac_f32_16x16x64_f16 v[130:133], v[156:159], v[248:255], v191
	s_nop 7
	v_cndmask_b32_e64 v156, v130, v131, s[0:1]
	v_exp_f32_e64 v158, -|v156|
	v_max_f32 v159, 0, v156
	v_add_f32 v158, 1.0, v158
	v_log_f32 v158, v158
	s_nop 0
	v_fma_mixlo_f16 v157, v158, 1.0, v159
	ds_write_b16 v148, v157
	v_mov_b32_e32 v192, v106
	v_mov_b32_e32 v193, v110
	v_mul_f32 v136, -2.0, v137
	s_nop 6
	ds_read_b128 v[208:211], v139
	s_waitcnt lgkmcnt(1)
	s_barrier
	ds_read_b128 v[212:215], v140
	ds_read_b128 v[216:219], v141
	s_waitcnt lgkmcnt(2)
	v_smfmac_f32_16x16x64_f16 v[192:195], v[208:211], v[6:13], v191
	ds_read_b128 v[220:223], v142
	s_waitcnt lgkmcnt(2)
	v_smfmac_f32_16x16x64_f16 v[192:195], v[212:215], v[14:21], v191
	s_waitcnt lgkmcnt(1)
	v_smfmac_f32_16x16x64_f16 v[192:195], v[216:219], v[26:33], v191
	s_waitcnt lgkmcnt(0)
	v_smfmac_f32_16x16x64_f16 v[192:195], v[220:223], v[34:41], v191
	s_nop 7
	v_cndmask_b32_e64 v156, v192, v193, s[0:1]
	v_exp_f32_e64 v158, -|v156|
	v_max_f32 v159, 0, v156
	v_add_f32 v158, 1.0, v158
	v_log_f32 v158, v158
	s_nop 0
	v_fma_mixlo_f16 v157, v158, 1.0, v159
	ds_write_b16 v149, v157
	v_mov_b32_e32 v200, v114
	v_mov_b32_e32 v201, v118
	v_mov_b32_e32 v204, v122
	v_mov_b32_e32 v205, v126
	s_nop 2
	ds_read_b128 v[208:211], v143
	s_waitcnt lgkmcnt(1)
	s_barrier
	ds_read_b128 v[212:215], v144
	ds_read_b128 v[216:219], v145
	s_waitcnt lgkmcnt(2)
	v_smfmac_f32_16x16x64_f16 v[200:203], v[208:211], v[42:49], v191
	ds_read_b128 v[220:223], v146
	v_smfmac_f32_16x16x64_f16 v[204:207], v[208:211], v[74:81], v191
	s_waitcnt lgkmcnt(2)
	v_smfmac_f32_16x16x64_f16 v[200:203], v[212:215], v[50:57], v191
	v_smfmac_f32_16x16x64_f16 v[204:207], v[212:215], v[82:89], v191
	s_waitcnt lgkmcnt(1)
	v_smfmac_f32_16x16x64_f16 v[200:203], v[216:219], v[58:65], v191
	v_smfmac_f32_16x16x64_f16 v[204:207], v[216:219], v[90:97], v191
	s_waitcnt lgkmcnt(0)
	v_smfmac_f32_16x16x64_f16 v[200:203], v[220:223], v[66:73], v191
	v_smfmac_f32_16x16x64_f16 v[204:207], v[220:223], v[98:105], v191
	s_nop 6
	v_cndmask_b32_e64 v172, v201, v200, s[6:7]
	v_cndmask_b32_e64 v172, v172, v204, s[0:1]
	v_cndmask_b32_e64 v172, v172, v205, s[4:5]
	v_exp_f32_e32 v172, v172
	s_nop 0
	v_add_f32_e32 v172, 1.0, v172
	v_rcp_f32_e32 v172, v172
	s_nop 0
	v_fmac_f32_e32 v137, v172, v136
	s_nop 1
	v_add_f32_dpp v136, v137, v137 quad_perm:[1,0,3,2] row_mask:0xf bank_mask:0xf bound_ctrl:1
	s_nop 1
	v_add_f32_dpp v136, v136, v136 quad_perm:[2,3,0,1] row_mask:0xf bank_mask:0xf bound_ctrl:1
	s_nop 1
	v_add_f32_dpp v136, v136, v136 row_half_mirror row_mask:0xf bank_mask:0xf bound_ctrl:1
	v_cvt_f16_f32_e32 v137, v136
	ds_write_b16 v150, v137
	s_waitcnt lgkmcnt(0)
	s_barrier
	ds_read_b128 v[156:159], v147
	ds_read_b32 v137, v134 offset:128
	v_add_f32_e32 v135, v135, v136
	s_waitcnt lgkmcnt(1)
	v_smfmac_f32_16x16x64_f16 v[130:133], v[156:159], v[248:255], v191
	s_nop 7
	v_cndmask_b32_e64 v156, v130, v131, s[0:1]
	v_exp_f32_e64 v158, -|v156|
	v_max_f32 v159, 0, v156
	v_add_f32 v158, 1.0, v158
	v_log_f32 v158, v158
	s_nop 0
	v_fma_mixlo_f16 v157, v158, 1.0, v159
	ds_write_b16 v148, v157
	v_mov_b32_e32 v192, v106
	v_mov_b32_e32 v193, v110
	v_mul_f32 v136, -2.0, v137
	s_nop 6
	ds_read_b128 v[208:211], v139
	s_waitcnt lgkmcnt(1)
	s_barrier
	ds_read_b128 v[212:215], v140
	ds_read_b128 v[216:219], v141
	s_waitcnt lgkmcnt(2)
	v_smfmac_f32_16x16x64_f16 v[192:195], v[208:211], v[6:13], v191
	ds_read_b128 v[220:223], v142
	s_waitcnt lgkmcnt(2)
	v_smfmac_f32_16x16x64_f16 v[192:195], v[212:215], v[14:21], v191
	s_waitcnt lgkmcnt(1)
	v_smfmac_f32_16x16x64_f16 v[192:195], v[216:219], v[26:33], v191
	s_waitcnt lgkmcnt(0)
	v_smfmac_f32_16x16x64_f16 v[192:195], v[220:223], v[34:41], v191
	s_nop 7
	v_cndmask_b32_e64 v156, v192, v193, s[0:1]
	v_exp_f32_e64 v158, -|v156|
	v_max_f32 v159, 0, v156
	v_add_f32 v158, 1.0, v158
	v_log_f32 v158, v158
	s_nop 0
	v_fma_mixlo_f16 v157, v158, 1.0, v159
	ds_write_b16 v149, v157
	v_mov_b32_e32 v200, v114
	v_mov_b32_e32 v201, v118
	v_mov_b32_e32 v204, v122
	v_mov_b32_e32 v205, v126
	s_nop 2
	ds_read_b128 v[208:211], v143
	s_waitcnt lgkmcnt(1)
	s_barrier
	ds_read_b128 v[212:215], v144
	ds_read_b128 v[216:219], v145
	s_waitcnt lgkmcnt(2)
	v_smfmac_f32_16x16x64_f16 v[200:203], v[208:211], v[42:49], v191
	ds_read_b128 v[220:223], v146
	v_smfmac_f32_16x16x64_f16 v[204:207], v[208:211], v[74:81], v191
	s_waitcnt lgkmcnt(2)
	v_smfmac_f32_16x16x64_f16 v[200:203], v[212:215], v[50:57], v191
	v_smfmac_f32_16x16x64_f16 v[204:207], v[212:215], v[82:89], v191
	s_waitcnt lgkmcnt(1)
	v_smfmac_f32_16x16x64_f16 v[200:203], v[216:219], v[58:65], v191
	v_smfmac_f32_16x16x64_f16 v[204:207], v[216:219], v[90:97], v191
	s_waitcnt lgkmcnt(0)
	v_smfmac_f32_16x16x64_f16 v[200:203], v[220:223], v[66:73], v191
	v_smfmac_f32_16x16x64_f16 v[204:207], v[220:223], v[98:105], v191
	s_nop 6
	v_cndmask_b32_e64 v172, v201, v200, s[6:7]
	v_cndmask_b32_e64 v172, v172, v204, s[0:1]
	v_cndmask_b32_e64 v172, v172, v205, s[4:5]
	v_exp_f32_e32 v172, v172
	s_nop 0
	v_add_f32_e32 v172, 1.0, v172
	v_rcp_f32_e32 v172, v172
	s_nop 0
	v_fmac_f32_e32 v137, v172, v136
	s_nop 1
	v_add_f32_dpp v136, v137, v137 quad_perm:[1,0,3,2] row_mask:0xf bank_mask:0xf bound_ctrl:1
	s_nop 1
	v_add_f32_dpp v136, v136, v136 quad_perm:[2,3,0,1] row_mask:0xf bank_mask:0xf bound_ctrl:1
	s_nop 1
	v_add_f32_dpp v136, v136, v136 row_half_mirror row_mask:0xf bank_mask:0xf bound_ctrl:1
	v_cvt_f16_f32_e32 v137, v136
	ds_write_b16 v150, v137
	s_waitcnt lgkmcnt(0)
	s_barrier
	ds_read_b128 v[156:159], v147
	ds_read_b32 v137, v134 offset:160
	v_add_f32_e32 v135, v135, v136
	s_waitcnt lgkmcnt(1)
	v_smfmac_f32_16x16x64_f16 v[130:133], v[156:159], v[248:255], v191
	s_nop 7
	v_cndmask_b32_e64 v156, v130, v131, s[0:1]
	v_exp_f32_e64 v158, -|v156|
	v_max_f32 v159, 0, v156
	v_add_f32 v158, 1.0, v158
	v_log_f32 v158, v158
	s_nop 0
	v_fma_mixlo_f16 v157, v158, 1.0, v159
	ds_write_b16 v148, v157
	v_mov_b32_e32 v192, v106
	v_mov_b32_e32 v193, v110
	v_mul_f32 v136, -2.0, v137
	s_nop 6
	ds_read_b128 v[208:211], v139
	s_waitcnt lgkmcnt(1)
	s_barrier
	ds_read_b128 v[212:215], v140
	ds_read_b128 v[216:219], v141
	s_waitcnt lgkmcnt(2)
	v_smfmac_f32_16x16x64_f16 v[192:195], v[208:211], v[6:13], v191
	ds_read_b128 v[220:223], v142
	s_waitcnt lgkmcnt(2)
	v_smfmac_f32_16x16x64_f16 v[192:195], v[212:215], v[14:21], v191
	s_waitcnt lgkmcnt(1)
	v_smfmac_f32_16x16x64_f16 v[192:195], v[216:219], v[26:33], v191
	s_waitcnt lgkmcnt(0)
	v_smfmac_f32_16x16x64_f16 v[192:195], v[220:223], v[34:41], v191
	s_nop 7
	v_cndmask_b32_e64 v156, v192, v193, s[0:1]
	v_exp_f32_e64 v158, -|v156|
	v_max_f32 v159, 0, v156
	v_add_f32 v158, 1.0, v158
	v_log_f32 v158, v158
	s_nop 0
	v_fma_mixlo_f16 v157, v158, 1.0, v159
	ds_write_b16 v149, v157
	v_mov_b32_e32 v200, v114
	v_mov_b32_e32 v201, v118
	v_mov_b32_e32 v204, v122
	v_mov_b32_e32 v205, v126
	s_nop 2
	ds_read_b128 v[208:211], v143
	s_waitcnt lgkmcnt(1)
	s_barrier
	ds_read_b128 v[212:215], v144
	ds_read_b128 v[216:219], v145
	s_waitcnt lgkmcnt(2)
	v_smfmac_f32_16x16x64_f16 v[200:203], v[208:211], v[42:49], v191
	ds_read_b128 v[220:223], v146
	v_smfmac_f32_16x16x64_f16 v[204:207], v[208:211], v[74:81], v191
	s_waitcnt lgkmcnt(2)
	v_smfmac_f32_16x16x64_f16 v[200:203], v[212:215], v[50:57], v191
	v_smfmac_f32_16x16x64_f16 v[204:207], v[212:215], v[82:89], v191
	s_waitcnt lgkmcnt(1)
	v_smfmac_f32_16x16x64_f16 v[200:203], v[216:219], v[58:65], v191
	v_smfmac_f32_16x16x64_f16 v[204:207], v[216:219], v[90:97], v191
	s_waitcnt lgkmcnt(0)
	v_smfmac_f32_16x16x64_f16 v[200:203], v[220:223], v[66:73], v191
	v_smfmac_f32_16x16x64_f16 v[204:207], v[220:223], v[98:105], v191
	s_nop 6
	v_cndmask_b32_e64 v172, v201, v200, s[6:7]
	v_cndmask_b32_e64 v172, v172, v204, s[0:1]
	v_cndmask_b32_e64 v172, v172, v205, s[4:5]
	v_exp_f32_e32 v172, v172
	s_nop 0
	v_add_f32_e32 v172, 1.0, v172
	v_rcp_f32_e32 v172, v172
	s_nop 0
	v_fmac_f32_e32 v137, v172, v136
	s_nop 1
	v_add_f32_dpp v136, v137, v137 quad_perm:[1,0,3,2] row_mask:0xf bank_mask:0xf bound_ctrl:1
	s_nop 1
	v_add_f32_dpp v136, v136, v136 quad_perm:[2,3,0,1] row_mask:0xf bank_mask:0xf bound_ctrl:1
	s_nop 1
	v_add_f32_dpp v136, v136, v136 row_half_mirror row_mask:0xf bank_mask:0xf bound_ctrl:1
	v_cvt_f16_f32_e32 v137, v136
	ds_write_b16 v150, v137
	s_waitcnt lgkmcnt(0)
	s_barrier
	ds_read_b128 v[156:159], v147
	ds_read_b32 v137, v134 offset:192
	v_add_f32_e32 v135, v135, v136
	s_waitcnt lgkmcnt(1)
	v_smfmac_f32_16x16x64_f16 v[130:133], v[156:159], v[248:255], v191
	s_nop 7
	v_cndmask_b32_e64 v152, v130, v131, s[0:1]
	v_exp_f32_e64 v158, -|v152|
	v_max_f32 v159, 0, v152
	v_add_f32 v158, 1.0, v158
	v_log_f32 v158, v158
	s_nop 0
	v_fma_mixlo_f16 v153, v158, 1.0, v159
	ds_write_b16 v148, v153
	v_mov_b32_e32 v192, v106
	v_mov_b32_e32 v193, v110
	v_mul_f32 v136, -2.0, v137
	s_nop 6
	ds_read_b128 v[208:211], v139
	s_waitcnt lgkmcnt(1)
	s_barrier
	ds_read_b128 v[212:215], v140
	ds_read_b128 v[216:219], v141
	s_waitcnt lgkmcnt(2)
	v_smfmac_f32_16x16x64_f16 v[192:195], v[208:211], v[6:13], v191
	ds_read_b128 v[220:223], v142
	s_waitcnt lgkmcnt(2)
	v_smfmac_f32_16x16x64_f16 v[192:195], v[212:215], v[14:21], v191
	s_waitcnt lgkmcnt(1)
	v_smfmac_f32_16x16x64_f16 v[192:195], v[216:219], v[26:33], v191
	s_waitcnt lgkmcnt(0)
	v_smfmac_f32_16x16x64_f16 v[192:195], v[220:223], v[34:41], v191
	s_nop 7
	v_cndmask_b32_e64 v152, v192, v193, s[0:1]
	v_exp_f32_e64 v158, -|v152|
	v_max_f32 v159, 0, v152
	v_add_f32 v158, 1.0, v158
	v_log_f32 v158, v158
	s_nop 0
	v_fma_mixlo_f16 v153, v158, 1.0, v159
	ds_write_b16 v149, v153
	v_mov_b32_e32 v200, v114
	v_mov_b32_e32 v201, v118
	v_mov_b32_e32 v204, v122
	v_mov_b32_e32 v205, v126
	s_nop 2
	ds_read_b128 v[208:211], v143
	s_waitcnt lgkmcnt(1)
	s_barrier
	ds_read_b128 v[212:215], v144
	ds_read_b128 v[216:219], v145
	s_waitcnt lgkmcnt(2)
	v_smfmac_f32_16x16x64_f16 v[200:203], v[208:211], v[42:49], v191
	ds_read_b128 v[220:223], v146
	v_smfmac_f32_16x16x64_f16 v[204:207], v[208:211], v[74:81], v191
	s_waitcnt lgkmcnt(2)
	v_smfmac_f32_16x16x64_f16 v[200:203], v[212:215], v[50:57], v191
	v_smfmac_f32_16x16x64_f16 v[204:207], v[212:215], v[82:89], v191
	s_waitcnt lgkmcnt(1)
	v_smfmac_f32_16x16x64_f16 v[200:203], v[216:219], v[58:65], v191
	v_smfmac_f32_16x16x64_f16 v[204:207], v[216:219], v[90:97], v191
	s_waitcnt lgkmcnt(0)
	v_smfmac_f32_16x16x64_f16 v[200:203], v[220:223], v[66:73], v191
	v_smfmac_f32_16x16x64_f16 v[204:207], v[220:223], v[98:105], v191
	s_nop 6
	v_cndmask_b32_e64 v152, v201, v200, s[6:7]
	v_cndmask_b32_e64 v152, v152, v204, s[0:1]
	v_cndmask_b32_e64 v152, v152, v205, s[4:5]
	v_exp_f32_e32 v152, v152
	s_nop 0
	v_add_f32_e32 v152, 1.0, v152
	v_rcp_f32_e32 v152, v152
	s_nop 0
	v_fmac_f32_e32 v137, v152, v136
	s_nop 1
	v_add_f32_dpp v136, v137, v137 quad_perm:[1,0,3,2] row_mask:0xf bank_mask:0xf bound_ctrl:1
	s_nop 1
	v_add_f32_dpp v136, v136, v136 quad_perm:[2,3,0,1] row_mask:0xf bank_mask:0xf bound_ctrl:1
	s_nop 1
	v_add_f32_dpp v136, v136, v136 row_half_mirror row_mask:0xf bank_mask:0xf bound_ctrl:1
	v_cvt_f16_f32_e32 v137, v136
	ds_write_b16 v150, v137
	s_waitcnt lgkmcnt(0)
	s_barrier
	ds_read_b128 v[158:161], v147
	v_add_f32_e32 v152, v135, v136
	ds_read_b32 v153, v134 offset:224
	s_addk_i32 s3, 0x100
	s_cmpk_eq_u32 s3, 0xfa20
	s_waitcnt lgkmcnt(1)
	v_smfmac_f32_16x16x64_f16 v[130:133], v[158:161], v[248:255], v191
	s_nop 7
	v_cndmask_b32_e64 v154, v130, v131, s[0:1]
	s_cbranch_scc0 .LBB0_21
	s_and_saveexec_b64 s[0:1], vcc
	ds_write_b32 v1, v152
	s_or_b64 exec, exec, s[0:1]
	v_cmp_gt_u32_e32 vcc, 10, v0
	s_waitcnt lgkmcnt(0)
	s_barrier
	s_and_saveexec_b64 s[0:1], vcc
	s_cbranch_execz .LBB0_28
	v_lshlrev_b32_e32 v1, 2, v0
	global_load_dword v1, v1, s[12:13]
	v_mov_b32_e32 v139, 0
	v_lshl_add_u64 v[2:3], s[10:11], 0, v[138:139]
	v_lshl_add_u64 v[2:3], v[2:3], 0, 28
	s_mov_b32 s0, 0
